# plus gather-index prefetch at unit start in the MoE gate/up GEMM (no vmcnt(0) drain in the last K iteration)
# speedup vs baseline: 1.0127x; 1.0026x over previous
.LBB0_923:
	s_lshl_b64 s[28:29], s[20:21], 17
	s_lshl_b32 s21, s20, 2
	s_add_i32 s21, s21, 0
	s_add_i32 s21, s21, 0x23c80
	v_lshl_or_b32 v2, v226, 8, v1
	s_add_u32 s28, s38, s28
	v_or_b32_e32 v222, v2, v206
	v_or_b32_e32 v228, v2, v207
	v_or_b32_e32 v2, 0x80, v2
	s_addc_u32 s29, s39, s29
	v_or_b32_e32 v229, v2, v206
	v_add_u32_e32 v230, v2, v207
	s_and_b64 vcc, exec, s[4:5]
	s_cbranch_vccz .Lgd_skip_a
	v_mov_b32_e32 v247, s21
	ds_read_b32 v247, v247 offset:160
	s_waitcnt lgkmcnt(0)
	v_add_u32_e32 v248, -1, v247
	v_min_i32_e32 v250, v222, v248
	v_ashrrev_i32_e32 v251, 31, v250
	v_lshl_add_u64 v[250:251], v[250:251], 2, s[28:29]
	global_load_dword v242, v[250:251], off
	v_min_i32_e32 v250, v228, v248
	v_ashrrev_i32_e32 v251, 31, v250
	v_lshl_add_u64 v[250:251], v[250:251], 2, s[28:29]
	global_load_dword v243, v[250:251], off
	v_min_i32_e32 v250, v229, v248
	v_ashrrev_i32_e32 v251, 31, v250
	v_lshl_add_u64 v[250:251], v[250:251], 2, s[28:29]
	global_load_dword v244, v[250:251], off
	v_min_i32_e32 v250, v230, v248
	v_ashrrev_i32_e32 v251, 31, v250
	v_lshl_add_u64 v[250:251], v[250:251], 2, s[28:29]
	global_load_dword v245, v[250:251], off
.Lgd_skip_a:
	s_add_u32 s25, s30, 0x100
	v_mov_b32_e32 v2, 0
	s_addc_u32 s27, s31, 0
	s_mov_b32 s64, -2
	s_mov_b64 s[30:31], s[16:17]
	v_mov_b32_e32 v3, v2
	v_mov_b32_e32 v4, v2
	v_mov_b32_e32 v5, v2
	v_mov_b32_e32 v6, v2
	v_mov_b32_e32 v7, v2
	v_mov_b32_e32 v8, v2
	v_mov_b32_e32 v9, v2
	v_mov_b32_e32 v10, v2
	v_mov_b32_e32 v11, v2
	v_mov_b32_e32 v12, v2
	v_mov_b32_e32 v13, v2
	v_mov_b32_e32 v14, v2
	v_mov_b32_e32 v15, v2
	v_mov_b32_e32 v16, v2
	v_mov_b32_e32 v17, v2
	v_mov_b32_e32 v34, v2
	v_mov_b32_e32 v35, v2
	v_mov_b32_e32 v36, v2
	v_mov_b32_e32 v37, v2
	v_mov_b32_e32 v38, v2
	v_mov_b32_e32 v39, v2
	v_mov_b32_e32 v40, v2
	v_mov_b32_e32 v41, v2
	v_mov_b32_e32 v42, v2
	v_mov_b32_e32 v43, v2
	v_mov_b32_e32 v44, v2
	v_mov_b32_e32 v45, v2
	v_mov_b32_e32 v46, v2
	v_mov_b32_e32 v47, v2
	v_mov_b32_e32 v48, v2
	v_mov_b32_e32 v49, v2
	v_mov_b32_e32 v18, v2
	v_mov_b32_e32 v19, v2
	v_mov_b32_e32 v20, v2
	v_mov_b32_e32 v21, v2
	v_mov_b32_e32 v22, v2
	v_mov_b32_e32 v23, v2
	v_mov_b32_e32 v24, v2
	v_mov_b32_e32 v25, v2
	v_mov_b32_e32 v26, v2
	v_mov_b32_e32 v27, v2
	v_mov_b32_e32 v28, v2
	v_mov_b32_e32 v29, v2
	v_mov_b32_e32 v30, v2
	v_mov_b32_e32 v31, v2
	v_mov_b32_e32 v32, v2
	v_mov_b32_e32 v33, v2
	v_mov_b32_e32 v50, v2
	v_mov_b32_e32 v51, v2
	v_mov_b32_e32 v52, v2
	v_mov_b32_e32 v53, v2
	v_mov_b32_e32 v54, v2
	v_mov_b32_e32 v55, v2
	v_mov_b32_e32 v56, v2
	v_mov_b32_e32 v57, v2
	v_mov_b32_e32 v58, v2
	v_mov_b32_e32 v59, v2
	v_mov_b32_e32 v60, v2
	v_mov_b32_e32 v61, v2
	v_mov_b32_e32 v62, v2
	v_mov_b32_e32 v63, v2
	v_mov_b32_e32 v64, v2
	v_mov_b32_e32 v65, v2
	v_mov_b32_e32 v66, v2
	v_mov_b32_e32 v67, v2
	v_mov_b32_e32 v68, v2
	v_mov_b32_e32 v69, v2
	v_mov_b32_e32 v70, v2
	v_mov_b32_e32 v71, v2
	v_mov_b32_e32 v72, v2
	v_mov_b32_e32 v73, v2
	v_mov_b32_e32 v74, v2
	v_mov_b32_e32 v75, v2
	v_mov_b32_e32 v76, v2
	v_mov_b32_e32 v77, v2
	v_mov_b32_e32 v78, v2
	v_mov_b32_e32 v79, v2
	v_mov_b32_e32 v80, v2
	v_mov_b32_e32 v81, v2
	v_mov_b32_e32 v98, v2
	v_mov_b32_e32 v99, v2
	v_mov_b32_e32 v100, v2
	v_mov_b32_e32 v101, v2
	v_mov_b32_e32 v102, v2
	v_mov_b32_e32 v103, v2
	v_mov_b32_e32 v104, v2
	v_mov_b32_e32 v105, v2
	v_mov_b32_e32 v106, v2
	v_mov_b32_e32 v107, v2
	v_mov_b32_e32 v108, v2
	v_mov_b32_e32 v109, v2
	v_mov_b32_e32 v110, v2
	v_mov_b32_e32 v111, v2
	v_mov_b32_e32 v112, v2
	v_mov_b32_e32 v113, v2
	v_mov_b32_e32 v82, v2
	v_mov_b32_e32 v83, v2
	v_mov_b32_e32 v84, v2
	v_mov_b32_e32 v85, v2
	v_mov_b32_e32 v86, v2
	v_mov_b32_e32 v87, v2
	v_mov_b32_e32 v88, v2
	v_mov_b32_e32 v89, v2
	v_mov_b32_e32 v90, v2
	v_mov_b32_e32 v91, v2
	v_mov_b32_e32 v92, v2
	v_mov_b32_e32 v93, v2
	v_mov_b32_e32 v94, v2
	v_mov_b32_e32 v95, v2
	v_mov_b32_e32 v96, v2
	v_mov_b32_e32 v97, v2
	v_mov_b32_e32 v114, v2
	v_mov_b32_e32 v115, v2
	v_mov_b32_e32 v116, v2
	v_mov_b32_e32 v117, v2
	v_mov_b32_e32 v118, v2
	v_mov_b32_e32 v119, v2
	v_mov_b32_e32 v120, v2
	v_mov_b32_e32 v121, v2
	v_mov_b32_e32 v122, v2
	v_mov_b32_e32 v123, v2
	v_mov_b32_e32 v124, v2
	v_mov_b32_e32 v125, v2
	v_mov_b32_e32 v126, v2
	v_mov_b32_e32 v127, v2
	v_mov_b32_e32 v128, v2
	v_mov_b32_e32 v129, v2
	s_branch .LBB0_926
.LBB0_924:
	v_mov_b32_e32 v198, v247
	v_mov_b32_e32 v200, v242
	v_mov_b32_e32 v202, v243
	v_mov_b32_e32 v203, v244
	v_mov_b32_e32 v204, v245
	v_cmp_lt_i32_e32 vcc, v222, v198
	v_mov_b32_e32 v201, v199
	v_lshlrev_b32_e32 v200, 11, v200
	v_lshlrev_b32_e32 v202, 11, v202
	v_cndmask_b32_e32 v200, v208, v200, vcc
	v_cmp_lt_i32_e32 vcc, v228, v198
	v_lshlrev_b32_e32 v203, 11, v203
	v_lshlrev_b32_e32 v204, 11, v204
	v_cndmask_b32_e32 v202, v208, v202, vcc
	v_cmp_lt_i32_e32 vcc, v229, v198
	v_or_b32_e32 v202, v202, v209
	s_nop 0
	v_cndmask_b32_e32 v203, v208, v203, vcc
	v_cmp_lt_i32_e32 vcc, v230, v198
	v_or_b32_e32 v198, v200, v209
	v_or_b32_e32 v200, v203, v209
	v_cndmask_b32_e32 v204, v208, v204, vcc
	v_or_b32_e32 v204, v204, v209

.LBB0_1534:
	s_lshl_b64 s[26:27], s[18:19], 17
	s_lshl_b32 s19, s18, 2
	s_add_i32 s19, s19, 0
	s_add_i32 s19, s19, 0x23c80
	v_lshl_or_b32 v2, v226, 8, v1
	s_add_u32 s26, s36, s26
	v_or_b32_e32 v222, v2, v206
	v_or_b32_e32 v228, v2, v207
	v_or_b32_e32 v2, 0x80, v2
	s_addc_u32 s27, s37, s27
	v_or_b32_e32 v229, v2, v206
	v_add_u32_e32 v230, v2, v207
	s_and_b64 vcc, exec, s[0:1]
	s_cbranch_vccz .Lgd_skip_b
	v_mov_b32_e32 v247, s19
	ds_read_b32 v247, v247 offset:160
	s_waitcnt lgkmcnt(0)
	v_add_u32_e32 v248, -1, v247
	v_min_i32_e32 v250, v222, v248
	v_ashrrev_i32_e32 v251, 31, v250
	v_lshl_add_u64 v[250:251], v[250:251], 2, s[26:27]
	global_load_dword v242, v[250:251], off
	v_min_i32_e32 v250, v228, v248
	v_ashrrev_i32_e32 v251, 31, v250
	v_lshl_add_u64 v[250:251], v[250:251], 2, s[26:27]
	global_load_dword v243, v[250:251], off
	v_min_i32_e32 v250, v229, v248
	v_ashrrev_i32_e32 v251, 31, v250
	v_lshl_add_u64 v[250:251], v[250:251], 2, s[26:27]
	global_load_dword v244, v[250:251], off
	v_min_i32_e32 v250, v230, v248
	v_ashrrev_i32_e32 v251, 31, v250
	v_lshl_add_u64 v[250:251], v[250:251], 2, s[26:27]
	global_load_dword v245, v[250:251], off
.Lgd_skip_b:
	s_add_u32 s23, s28, 0x100
	v_mov_b32_e32 v2, 0
	s_addc_u32 s25, s29, 0
	s_mov_b32 s62, -2
	s_mov_b64 s[28:29], s[14:15]
	v_mov_b32_e32 v3, v2
	v_mov_b32_e32 v4, v2
	v_mov_b32_e32 v5, v2
	v_mov_b32_e32 v6, v2
	v_mov_b32_e32 v7, v2
	v_mov_b32_e32 v8, v2
	v_mov_b32_e32 v9, v2
	v_mov_b32_e32 v10, v2
	v_mov_b32_e32 v11, v2
	v_mov_b32_e32 v12, v2
	v_mov_b32_e32 v13, v2
	v_mov_b32_e32 v14, v2
	v_mov_b32_e32 v15, v2
	v_mov_b32_e32 v16, v2
	v_mov_b32_e32 v17, v2
	v_mov_b32_e32 v34, v2
	v_mov_b32_e32 v35, v2
	v_mov_b32_e32 v36, v2
	v_mov_b32_e32 v37, v2
	v_mov_b32_e32 v38, v2
	v_mov_b32_e32 v39, v2
	v_mov_b32_e32 v40, v2
	v_mov_b32_e32 v41, v2
	v_mov_b32_e32 v42, v2
	v_mov_b32_e32 v43, v2
	v_mov_b32_e32 v44, v2
	v_mov_b32_e32 v45, v2
	v_mov_b32_e32 v46, v2
	v_mov_b32_e32 v47, v2
	v_mov_b32_e32 v48, v2
	v_mov_b32_e32 v49, v2
	v_mov_b32_e32 v18, v2
	v_mov_b32_e32 v19, v2
	v_mov_b32_e32 v20, v2
	v_mov_b32_e32 v21, v2
	v_mov_b32_e32 v22, v2
	v_mov_b32_e32 v23, v2
	v_mov_b32_e32 v24, v2
	v_mov_b32_e32 v25, v2
	v_mov_b32_e32 v26, v2
	v_mov_b32_e32 v27, v2
	v_mov_b32_e32 v28, v2
	v_mov_b32_e32 v29, v2
	v_mov_b32_e32 v30, v2
	v_mov_b32_e32 v31, v2
	v_mov_b32_e32 v32, v2
	v_mov_b32_e32 v33, v2
	v_mov_b32_e32 v50, v2
	v_mov_b32_e32 v51, v2
	v_mov_b32_e32 v52, v2
	v_mov_b32_e32 v53, v2
	v_mov_b32_e32 v54, v2
	v_mov_b32_e32 v55, v2
	v_mov_b32_e32 v56, v2
	v_mov_b32_e32 v57, v2
	v_mov_b32_e32 v58, v2
	v_mov_b32_e32 v59, v2
	v_mov_b32_e32 v60, v2
	v_mov_b32_e32 v61, v2
	v_mov_b32_e32 v62, v2
	v_mov_b32_e32 v63, v2
	v_mov_b32_e32 v64, v2
	v_mov_b32_e32 v65, v2
	v_mov_b32_e32 v66, v2
	v_mov_b32_e32 v67, v2
	v_mov_b32_e32 v68, v2
	v_mov_b32_e32 v69, v2
	v_mov_b32_e32 v70, v2
	v_mov_b32_e32 v71, v2
	v_mov_b32_e32 v72, v2
	v_mov_b32_e32 v73, v2
	v_mov_b32_e32 v74, v2
	v_mov_b32_e32 v75, v2
	v_mov_b32_e32 v76, v2
	v_mov_b32_e32 v77, v2
	v_mov_b32_e32 v78, v2
	v_mov_b32_e32 v79, v2
	v_mov_b32_e32 v80, v2
	v_mov_b32_e32 v81, v2
	v_mov_b32_e32 v98, v2
	v_mov_b32_e32 v99, v2
	v_mov_b32_e32 v100, v2
	v_mov_b32_e32 v101, v2
	v_mov_b32_e32 v102, v2
	v_mov_b32_e32 v103, v2
	v_mov_b32_e32 v104, v2
	v_mov_b32_e32 v105, v2
	v_mov_b32_e32 v106, v2
	v_mov_b32_e32 v107, v2
	v_mov_b32_e32 v108, v2
	v_mov_b32_e32 v109, v2
	v_mov_b32_e32 v110, v2
	v_mov_b32_e32 v111, v2
	v_mov_b32_e32 v112, v2
	v_mov_b32_e32 v113, v2
	v_mov_b32_e32 v82, v2
	v_mov_b32_e32 v83, v2
	v_mov_b32_e32 v84, v2
	v_mov_b32_e32 v85, v2
	v_mov_b32_e32 v86, v2
	v_mov_b32_e32 v87, v2
	v_mov_b32_e32 v88, v2
	v_mov_b32_e32 v89, v2
	v_mov_b32_e32 v90, v2
	v_mov_b32_e32 v91, v2
	v_mov_b32_e32 v92, v2
	v_mov_b32_e32 v93, v2
	v_mov_b32_e32 v94, v2
	v_mov_b32_e32 v95, v2
	v_mov_b32_e32 v96, v2
	v_mov_b32_e32 v97, v2
	v_mov_b32_e32 v114, v2
	v_mov_b32_e32 v115, v2
	v_mov_b32_e32 v116, v2
	v_mov_b32_e32 v117, v2
	v_mov_b32_e32 v118, v2
	v_mov_b32_e32 v119, v2
	v_mov_b32_e32 v120, v2
	v_mov_b32_e32 v121, v2
	v_mov_b32_e32 v122, v2
	v_mov_b32_e32 v123, v2
	v_mov_b32_e32 v124, v2
	v_mov_b32_e32 v125, v2
	v_mov_b32_e32 v126, v2
	v_mov_b32_e32 v127, v2
	v_mov_b32_e32 v128, v2
	v_mov_b32_e32 v129, v2
	s_branch .LBB0_1537
